# static s_setprio 1 for waves 4-7 inside the MLA DSTEP loop, on top of balanced GEMM DMA + MLA reschedule
# baseline (speedup 1.0000x reference)
.LBB0_557:
	v_lshlrev_b32_e32 v2, 4, v2
	s_lshl_b32 s33, s21, 10
	v_cndmask_b32_e64 v2, 0, v2, s[6:7]
	s_lshl_b32 s64, s20, 10
	s_ashr_i32 s49, s48, 31
	s_mul_i32 s7, s48, 0x1800
	v_lshlrev_b32_e32 v4, 4, v4
	s_mul_hi_i32 s6, s48, 0x1800
	s_add_u32 s7, s3, s7
	v_cndmask_b32_e64 v4, 0, v4, s[10:11]
	s_addc_u32 s10, s61, s6
	s_ashr_i32 s11, s87, 31
	s_add_u32 s6, s7, s87
	s_addc_u32 s7, s10, s11
	s_and_b32 s10, s19, 0x3fffffc0
	s_lshl_b32 s10, s10, 2
	s_add_i32 s51, s10, 0
	s_add_i32 s51, s51, 0x1e000
	s_lshl_b32 s65, s18, 10
	v_add_u32_e32 v211, v2, v3
	v_lshlrev_b32_e32 v2, 4, v6
	s_and_b64 s[10:11], s[52:53], exec
	v_cndmask_b32_e64 v2, 0, v2, s[14:15]
	s_cselect_b32 s11, s57, s59
	s_cselect_b32 s10, s56, s58
	s_mov_b32 s14, m0
	s_mov_b32 m0, s65
	s_nop 0
	global_load_lds_dwordx4 v211, s[10:11]
	s_mov_b32 m0, s14
	v_add_u32_e32 v210, v4, v5
	s_mov_b32 s10, m0
	s_mov_b32 m0, s64
	s_nop 0
	global_load_lds_dwordx4 v210, s[12:13]
	s_mov_b32 m0, s10
	v_add_u32_e32 v212, v2, v10
	s_mov_b32 s10, m0
	s_mov_b32 m0, s33
	s_nop 0
	global_load_lds_dwordx4 v212, s[12:13]
	s_mov_b32 m0, s10
	s_add_u32 s12, s56, 0x80000
	s_addc_u32 s13, s57, 0
	s_add_u32 s14, s58, 0x2000
	s_addc_u32 s15, s59, 0
	s_and_b64 s[10:11], s[52:53], exec
	s_cselect_b32 s11, s13, s15
	s_cselect_b32 s10, s12, s14
	s_add_i32 s16, s65, 0x5c00
	s_mov_b32 s17, m0
	s_mov_b32 m0, s16
	s_nop 0
	global_load_lds_dwordx4 v211, s[10:11]
	s_mov_b32 m0, s17
	s_and_b64 s[10:11], exec, s[54:55]
	v_and_b32_e32 v206, 31, v9
	s_cselect_b32 s11, s13, s15
	s_cselect_b32 s10, s12, s14
	s_lshl_b32 s50, s9, 5
	v_lshrrev_b32_e32 v207, 5, v8
	v_or_b32_e32 v4, s50, v206
	v_mov_b64_e32 v[2:3], s[6:7]
	s_movk_i32 s6, 0x1800
	s_add_i32 s12, s64, 0x5c00
	s_mov_b32 s13, m0
	s_mov_b32 m0, s12
	s_nop 0
	global_load_lds_dwordx4 v210, s[10:11]
	s_mov_b32 m0, s13
	v_mad_i64_i32 v[2:3], s[6:7], v4, s6, v[2:3]
	v_lshlrev_b32_e32 v204, 6, v207
	s_add_i32 s12, s33, 0x5c00
	s_mov_b32 s13, m0
	s_mov_b32 m0, s12
	s_nop 0
	global_load_lds_dwordx4 v212, s[10:11]
	s_mov_b32 m0, s13
	v_lshl_add_u64 v[2:3], v[2:3], 0, v[204:205]
	global_load_dwordx4 v[4:7], v[2:3], off
	global_load_dwordx4 v[10:13], v[2:3], off offset:16
	global_load_dwordx4 v[14:17], v[2:3], off offset:32
	global_load_dwordx4 v[18:21], v[2:3], off offset:48
	global_load_dwordx4 v[22:25], v[2:3], off offset:128
	global_load_dwordx4 v[26:29], v[2:3], off offset:144
	global_load_dwordx4 v[30:33], v[2:3], off offset:160
	global_load_dwordx4 v[34:37], v[2:3], off offset:176
	s_add_i32 s6, s50, s48
	v_and_b32_e32 v130, 32, v9
	v_add_u32_e32 v9, s6, v206
	v_lshlrev_b32_e32 v213, 2, v130
	v_cmp_gt_u32_e32 vcc, 32, v8
	s_add_u32 s9, s56, 0x100000
	s_addc_u32 s10, s57, 0
	s_add_u32 s11, s58, 0x4000
	s_addc_u32 s12, s59, 0
	s_and_b64 s[6:7], s[52:53], exec
	v_mad_u32_u24 v204, v206, s88, v130
	s_mov_b32 s22, s8
	s_mov_b32 s23, s8
	s_mov_b32 s15, s8
	s_mov_b32 s16, s8
	s_mov_b32 s17, s8
	s_mov_b32 s18, s8
	s_mov_b32 s19, s8
	s_mov_b32 s20, s8
	s_mov_b32 s21, s8
	s_waitcnt vmcnt(7)
	v_lshlrev_b32_e32 v183, 16, v4
	v_and_b32_e32 v181, 0xffff0000, v4
	v_lshlrev_b32_e32 v182, 16, v5
	v_and_b32_e32 v179, 0xffff0000, v5
	v_mov_b64_e32 v[4:5], s[42:43]
	s_waitcnt vmcnt(6)
	v_lshlrev_b32_e32 v176, 16, v10
	v_and_b32_e32 v173, 0xffff0000, v10
	v_lshlrev_b32_e32 v174, 16, v11
	v_and_b32_e32 v171, 0xffff0000, v11
	v_mad_i64_i32 v[10:11], s[6:7], v9, s89, v[4:5]
	v_lshlrev_b32_e32 v180, 16, v6
	v_and_b32_e32 v177, 0xffff0000, v6
	v_lshlrev_b32_e32 v178, 16, v7
	v_and_b32_e32 v175, 0xffff0000, v7
	v_lshlrev_b32_e32 v172, 16, v12
	v_and_b32_e32 v169, 0xffff0000, v12
	v_lshlrev_b32_e32 v170, 16, v13
	v_and_b32_e32 v167, 0xffff0000, v13
	s_waitcnt vmcnt(5)
	v_lshlrev_b32_e32 v168, 16, v14
	v_and_b32_e32 v165, 0xffff0000, v14
	v_lshlrev_b32_e32 v166, 16, v15
	v_and_b32_e32 v164, 0xffff0000, v15
	v_lshlrev_b32_e32 v163, 16, v16
	v_and_b32_e32 v161, 0xffff0000, v16
	v_lshlrev_b32_e32 v160, 16, v17
	v_and_b32_e32 v159, 0xffff0000, v17
	s_waitcnt vmcnt(4)
	v_lshlrev_b32_e32 v158, 16, v18
	v_and_b32_e32 v157, 0xffff0000, v18
	v_lshlrev_b32_e32 v156, 16, v19
	v_and_b32_e32 v155, 0xffff0000, v19
	v_lshlrev_b32_e32 v154, 16, v20
	v_and_b32_e32 v153, 0xffff0000, v20
	v_lshlrev_b32_e32 v152, 16, v21
	v_and_b32_e32 v151, 0xffff0000, v21
	global_load_dwordx4 v[4:7], v[10:11], off
	s_nop 0
	global_load_dwordx4 v[10:13], v[10:11], off offset:16
	s_nop 0
	global_load_dwordx4 v[64:67], v[2:3], off offset:288
	global_load_dwordx4 v[112:115], v[2:3], off offset:304
	global_load_dwordx4 v[76:79], v[2:3], off offset:256
	global_load_dwordx4 v[116:119], v[2:3], off offset:272
	global_load_dwordx4 v[120:123], v213, s[38:39] offset:608
	global_load_dwordx4 v[102:105], v213, s[38:39] offset:624
	global_load_dwordx4 v[14:17], v213, s[38:39] offset:560
	global_load_dwordx4 v[18:21], v213, s[38:39] offset:544
	v_mul_f32_e32 v202, v181, v181
	v_fmac_f32_e32 v202, v183, v183
	v_fmac_f32_e32 v202, v182, v182
	v_fmac_f32_e32 v202, v179, v179
	v_fmac_f32_e32 v202, v180, v180
	v_fmac_f32_e32 v202, v177, v177
	v_fmac_f32_e32 v202, v178, v178
	v_fmac_f32_e32 v202, v175, v175
	v_fmac_f32_e32 v202, v176, v176
	v_fmac_f32_e32 v202, v173, v173
	v_fmac_f32_e32 v202, v174, v174
	v_fmac_f32_e32 v202, v171, v171
	v_fmac_f32_e32 v202, v172, v172
	v_fmac_f32_e32 v202, v169, v169
	v_fmac_f32_e32 v202, v170, v170
	v_fmac_f32_e32 v202, v167, v167
	v_fmac_f32_e32 v202, v168, v168
	global_load_dwordx4 v[72:75], v213, s[38:39] offset:48
	global_load_dwordx4 v[80:83], v213, s[38:39] offset:32
	global_load_dwordx4 v[84:87], v213, s[38:39] offset:16
	global_load_dwordx4 v[88:91], v213, s[38:39]
	global_load_dwordx4 v[52:55], v213, s[38:39] offset:112
	global_load_dwordx4 v[56:59], v213, s[38:39] offset:96
	global_load_dwordx4 v[60:63], v213, s[38:39] offset:80
	global_load_dwordx4 v[68:71], v213, s[38:39] offset:64
	global_load_dwordx4 v[44:47], v213, s[38:39] offset:512
	global_load_dwordx4 v[40:43], v213, s[38:39] offset:528
	global_load_dwordx4 v[48:51], v213, s[38:39] offset:576
	global_load_dwordx4 v[192:195], v213, s[38:39] offset:592
	v_fmac_f32_e32 v202, v165, v165
	v_fmac_f32_e32 v202, v166, v166
	v_fmac_f32_e32 v202, v164, v164
	v_fmac_f32_e32 v202, v163, v163
	v_fmac_f32_e32 v202, v161, v161
	v_fmac_f32_e32 v202, v160, v160
	v_fmac_f32_e32 v202, v159, v159
	v_fmac_f32_e32 v202, v158, v158
	v_fmac_f32_e32 v202, v157, v157
	v_fmac_f32_e32 v202, v156, v156
	v_fmac_f32_e32 v202, v155, v155
	v_fmac_f32_e32 v202, v154, v154
	v_fmac_f32_e32 v202, v153, v153
	v_fmac_f32_e32 v202, v152, v152
	s_waitcnt vmcnt(25)
	v_lshlrev_b32_e32 v150, 16, v22
	v_fmac_f32_e32 v202, v151, v151
	v_and_b32_e32 v149, 0xffff0000, v22
	v_fmac_f32_e32 v202, v150, v150
	v_lshlrev_b32_e32 v148, 16, v23
	v_fmac_f32_e32 v202, v149, v149
	v_and_b32_e32 v147, 0xffff0000, v23
	v_fmac_f32_e32 v202, v148, v148
	v_lshlrev_b32_e32 v146, 16, v24
	v_fmac_f32_e32 v202, v147, v147
	v_and_b32_e32 v145, 0xffff0000, v24
	v_fmac_f32_e32 v202, v146, v146
	v_lshlrev_b32_e32 v144, 16, v25
	v_fmac_f32_e32 v202, v145, v145
	v_and_b32_e32 v143, 0xffff0000, v25
	v_fmac_f32_e32 v202, v144, v144
	s_waitcnt vmcnt(24)
	v_lshlrev_b32_e32 v142, 16, v26
	v_fmac_f32_e32 v202, v143, v143
	v_and_b32_e32 v141, 0xffff0000, v26
	v_fmac_f32_e32 v202, v142, v142
	v_lshlrev_b32_e32 v140, 16, v27
	v_fmac_f32_e32 v202, v141, v141
	v_and_b32_e32 v139, 0xffff0000, v27
	v_fmac_f32_e32 v202, v140, v140
	v_lshlrev_b32_e32 v138, 16, v28
	v_fmac_f32_e32 v202, v139, v139
	v_and_b32_e32 v137, 0xffff0000, v28
	v_fmac_f32_e32 v202, v138, v138
	v_lshlrev_b32_e32 v136, 16, v29
	v_fmac_f32_e32 v202, v137, v137
	v_and_b32_e32 v135, 0xffff0000, v29
	v_fmac_f32_e32 v202, v136, v136
	s_waitcnt vmcnt(23)
	v_lshlrev_b32_e32 v134, 16, v30
	v_fmac_f32_e32 v202, v135, v135
	v_and_b32_e32 v133, 0xffff0000, v30
	v_fmac_f32_e32 v202, v134, v134
	v_lshlrev_b32_e32 v132, 16, v31
	v_fmac_f32_e32 v202, v133, v133
	v_and_b32_e32 v131, 0xffff0000, v31
	v_fmac_f32_e32 v202, v132, v132
	v_lshlrev_b32_e32 v129, 16, v32
	v_fmac_f32_e32 v202, v131, v131
	v_and_b32_e32 v128, 0xffff0000, v32
	v_fmac_f32_e32 v202, v129, v129
	v_lshlrev_b32_e32 v127, 16, v33
	v_fmac_f32_e32 v202, v128, v128
	v_and_b32_e32 v126, 0xffff0000, v33
	v_fmac_f32_e32 v202, v127, v127
	s_waitcnt vmcnt(22)
	v_lshlrev_b32_e32 v191, 16, v34
	v_fmac_f32_e32 v202, v126, v126
	v_and_b32_e32 v190, 0xffff0000, v34
	v_fmac_f32_e32 v202, v191, v191
	v_lshlrev_b32_e32 v189, 16, v35
	v_fmac_f32_e32 v202, v190, v190
	v_and_b32_e32 v188, 0xffff0000, v35
	v_fmac_f32_e32 v202, v189, v189
	v_lshlrev_b32_e32 v187, 16, v36
	v_fmac_f32_e32 v202, v188, v188
	v_and_b32_e32 v186, 0xffff0000, v36
	v_fmac_f32_e32 v202, v187, v187
	v_lshlrev_b32_e32 v185, 16, v37
	v_fmac_f32_e32 v202, v186, v186
	v_and_b32_e32 v184, 0xffff0000, v37
	v_fmac_f32_e32 v202, v185, v185
	s_waitcnt vmcnt(17)
	v_lshlrev_b32_e32 v125, 16, v76
	v_lshlrev_b32_e32 v124, 16, v64
	v_fmac_f32_e32 v202, v184, v184
	s_waitcnt vmcnt(16)
	v_lshlrev_b32_e32 v31, 16, v119
	v_lshlrev_b32_e32 v30, 16, v115
	s_waitcnt vmcnt(13)
	v_mov_b32_e32 v93, v16
	v_and_b32_e32 v95, 0xffff0000, v119
	v_and_b32_e32 v94, 0xffff0000, v115
	v_mov_b32_e32 v16, v105
	v_lshlrev_b32_e32 v97, 16, v118
	v_lshlrev_b32_e32 v96, 16, v114
	v_mov_b32_e32 v98, v102
	v_mov_b32_e32 v99, v14
	v_and_b32_e32 v101, 0xffff0000, v118
	v_and_b32_e32 v100, 0xffff0000, v114
	v_mov_b32_e32 v14, v103
	v_lshlrev_b32_e32 v103, 16, v117
	v_lshlrev_b32_e32 v102, 16, v113
	s_waitcnt vmcnt(12)
	v_mov_b32_e32 v105, v20
	v_and_b32_e32 v107, 0xffff0000, v117
	v_and_b32_e32 v106, 0xffff0000, v113
	v_mov_b32_e32 v20, v123
	v_lshlrev_b32_e32 v109, 16, v116
	v_mov_b32_e32 v111, v18
	v_and_b32_e32 v113, 0xffff0000, v116
	v_mov_b32_e32 v18, v121
	v_lshlrev_b32_e32 v115, 16, v79
	v_lshlrev_b32_e32 v114, 16, v67
	v_and_b32_e32 v117, 0xffff0000, v79
	v_and_b32_e32 v116, 0xffff0000, v67
	v_lshlrev_b32_e32 v119, 16, v78
	v_lshlrev_b32_e32 v118, 16, v66
	v_and_b32_e32 v79, 0xffff0000, v78
	v_and_b32_e32 v78, 0xffff0000, v66
	v_lshlrev_b32_e32 v121, 16, v77
	v_and_b32_e32 v123, 0xffff0000, v77
	v_and_b32_e32 v77, 0xffff0000, v76
	v_pk_mul_f32 v[66:67], v[124:125], v[124:125]
	v_and_b32_e32 v76, 0xffff0000, v64
	v_mov_b32_e32 v92, v104
	v_mov_b32_e32 v104, v122
	v_mov_b32_e32 v110, v120
	v_lshlrev_b32_e32 v120, 16, v65
	v_and_b32_e32 v122, 0xffff0000, v65
	v_add_f32_e32 v65, v67, v202
	v_pk_mul_f32 v[202:203], v[76:77], v[76:77]
	v_pk_mul_f32 v[198:199], v[120:121], v[120:121]
	v_add_f32_e32 v64, v203, v65
	v_pk_mul_f32 v[200:201], v[122:123], v[122:123]
	v_add_f32_e32 v64, v199, v64
	v_pk_mul_f32 v[196:197], v[118:119], v[118:119]
	v_add_f32_e32 v64, v201, v64
	v_pk_mul_f32 v[220:221], v[78:79], v[78:79]
	v_add_f32_e32 v64, v197, v64
	v_pk_mul_f32 v[216:217], v[114:115], v[114:115]
	v_add_f32_e32 v64, v221, v64
	v_lshlrev_b32_e32 v108, 16, v112
	v_pk_mul_f32 v[218:219], v[116:117], v[116:117]
	v_add_f32_e32 v64, v217, v64
	v_pk_mul_f32 v[214:215], v[108:109], v[108:109]
	v_and_b32_e32 v112, 0xffff0000, v112
	v_add_f32_e32 v64, v219, v64
	v_pk_mul_f32 v[228:229], v[112:113], v[112:113]
	v_add_f32_e32 v64, v215, v64
	v_pk_mul_f32 v[224:225], v[102:103], v[102:103]
	v_add_f32_e32 v64, v229, v64
	v_pk_mul_f32 v[226:227], v[106:107], v[106:107]
	v_add_f32_e32 v64, v225, v64
	v_pk_mul_f32 v[222:223], v[96:97], v[96:97]
	v_add_f32_e32 v64, v227, v64
	v_pk_mul_f32 v[232:233], v[100:101], v[100:101]
	v_add_f32_e32 v64, v223, v64
	v_pk_mul_f32 v[208:209], v[30:31], v[30:31]
	v_add_f32_e32 v64, v233, v64
	v_pk_mul_f32 v[230:231], v[94:95], v[94:95]
	v_add_f32_e32 v64, v209, v64
	v_add_f32_e32 v64, v231, v64
	v_add_f32_e32 v197, v66, v64
	v_add_f32_e32 v197, v202, v197
	v_add_f32_e32 v197, v198, v197
	v_mov_b32_e32 v2, v4
	v_mov_b32_e32 v3, v10
	v_mov_b32_e32 v10, v5
	v_mov_b32_e32 v4, v6
	v_mov_b32_e32 v5, v12
	v_mov_b32_e32 v12, v7
	v_add_f32_e32 v197, v200, v197
	v_pk_add_f32 v[2:3], v[2:3], v[10:11]
	v_pk_add_f32 v[4:5], v[4:5], v[12:13]
	v_add_f32_e32 v209, v196, v197
	v_pk_add_f32 v[2:3], v[2:3], v[4:5]
	v_add_f32_e32 v209, v220, v209
	v_add_f32_e32 v2, v2, v3
	v_add_f32_e32 v209, v216, v209
	v_fmamk_f32 v2, v2, 0x3b000000, v1
	v_add_f32_e32 v209, v218, v209
	v_rsq_f32_e32 v234, v2
	v_and_b32_e32 v2, 63, v9
	v_bfe_u32 v3, v9, 6, 8
	v_add_f32_e32 v209, v214, v209
	v_cndmask_b32_e32 v2, v2, v3, vcc
	v_add_f32_e32 v209, v228, v209
	v_lshlrev_b32_e32 v236, 6, v2
	v_add_f32_e32 v209, v224, v209
	global_load_dwordx4 v[36:39], v236, s[40:41]
	global_load_dwordx4 v[22:25], v236, s[40:41] offset:16
	global_load_dwordx4 v[6:9], v236, s[40:41] offset:32
	global_load_dwordx4 v[2:5], v236, s[40:41] offset:48
	global_load_dwordx4 v[26:29], v236, s[44:45] offset:16
	global_load_dwordx4 v[10:13], v236, s[44:45] offset:32
	global_load_dwordx4 v[32:35], v236, s[44:45] offset:48
	global_load_dwordx4 v[64:67], v236, s[44:45]
	global_load_dwordx4 v[196:199], v213, s[38:39] offset:304
	global_load_dwordx4 v[200:203], v213, s[38:39] offset:288
	global_load_dwordx4 v[214:217], v213, s[38:39] offset:272
	global_load_dwordx4 v[218:221], v213, s[38:39] offset:256
	v_add_f32_e32 v209, v226, v209
	v_add_f32_e32 v209, v222, v209
	v_add_f32_e32 v209, v232, v209
	v_add_f32_e32 v208, v208, v209
	v_add_f32_e32 v230, v230, v208
	s_waitcnt vmcnt(12)
	v_mov_b32_e32 v208, v194
	v_mov_b32_e32 v194, v230
	s_nop 1
	v_permlane32_swap_b32_e32 v230, v194
	v_mul_f32_e32 v235, v234, v234
	v_add_f32_e32 v194, v230, v194
	v_mul_f32_e32 v194, v194, v235
	v_fmamk_f32 v194, v194, 0x3baaaaab, v1
	v_rsq_f32_e32 v230, v194
	v_mov_b32_e32 v194, v192
	global_load_dwordx4 v[222:225], v213, s[38:39] offset:368
	global_load_dwordx4 v[226:229], v213, s[38:39] offset:352
	v_mov_b32_e32 v209, v42
	v_mul_f32_e32 v192, v234, v230
	v_mul_f32_e32 v192, 0x3ea53555, v192
	v_mul_f32_e32 v231, v80, v192
	v_mul_f32_e32 v232, v81, v192
	v_mul_f32_e32 v233, v82, v192
	v_mul_f32_e32 v234, v83, v192
	v_mul_f32_e32 v235, v72, v192
	v_mul_f32_e32 v236, v73, v192
	v_mul_f32_e32 v237, v74, v192
	v_mul_f32_e32 v238, v75, v192
	global_load_dwordx4 v[72:75], v213, s[38:39] offset:336
	global_load_dwordx4 v[80:83], v213, s[38:39] offset:320
	v_mov_b32_e32 v42, v195
	v_mov_b32_e32 v195, v40
	v_mov_b32_e32 v40, v193
	v_mul_f32_e32 v193, v85, v192
	v_mul_f32_e32 v177, v193, v177
	v_mul_f32_e32 v193, v232, v173
	v_mov_b32_e32 v173, v46
	v_mov_b32_e32 v46, v51
	v_mov_b32_e32 v51, v44
	v_mul_f32_e32 v44, v60, v192
	v_mul_f32_e32 v163, v44, v163
	v_mul_f32_e32 v44, v61, v192
	v_mul_f32_e32 v161, v44, v161
	v_mul_f32_e32 v44, v62, v192
	v_mul_f32_e32 v160, v44, v160
	v_mul_f32_e32 v44, v63, v192
	v_mul_f32_e32 v159, v44, v159
	v_mul_f32_e32 v44, v56, v192
	v_mul_f32_e32 v158, v44, v158
	v_mul_f32_e32 v44, v57, v192
	v_mul_f32_e32 v157, v44, v157
	v_mul_f32_e32 v44, v58, v192
	v_mul_f32_e32 v156, v44, v156
	v_mul_f32_e32 v44, v59, v192
	v_mul_f32_e32 v155, v44, v155
	v_mul_f32_e32 v44, v52, v192
	v_mul_f32_e32 v154, v44, v154
	v_mul_f32_e32 v44, v53, v192
	v_mul_f32_e32 v153, v44, v153
	v_mul_f32_e32 v44, v54, v192
	v_mul_f32_e32 v152, v44, v152
	v_mul_f32_e32 v44, v55, v192
	v_mul_f32_e32 v151, v44, v151
	v_pk_mul_f32 v[40:41], v[192:193], v[40:41] op_sel_hi:[0,1]
	v_pk_mul_f32 v[54:55], v[40:41], v[78:79]
	v_pk_mul_f32 v[40:41], v[192:193], v[208:209] op_sel_hi:[0,1]
	v_pk_mul_f32 v[56:57], v[40:41], v[114:115]
	v_pk_mul_f32 v[40:41], v[192:193], v[42:43] op_sel_hi:[0,1]
	v_pk_mul_f32 v[42:43], v[40:41], v[116:117]
	v_pk_mul_f32 v[40:41], v[192:193], v[110:111] op_sel_hi:[0,1]
	v_pk_mul_f32 v[58:59], v[40:41], v[108:109]
	v_pk_mul_f32 v[40:41], v[192:193], v[104:105] op_sel_hi:[0,1]
	v_mul_f32_e32 v176, v231, v176
	v_mul_f32_e32 v231, v235, v172
	v_mov_b32_e32 v172, v50
	v_mov_b32_e32 v50, v48
	v_pk_mul_f32 v[60:61], v[40:41], v[102:103]
	v_pk_mul_f32 v[40:41], v[192:193], v[98:99] op_sel_hi:[0,1]
	v_pk_mul_f32 v[50:51], v[192:193], v[50:51] op_sel_hi:[0,1]
	v_pk_mul_f32 v[62:63], v[40:41], v[96:97]
	v_pk_mul_f32 v[40:41], v[192:193], v[92:93] op_sel_hi:[0,1]
	s_waitcnt vmcnt(4)
	v_mul_f32_e32 v44, v218, v192
	v_mul_f32_e32 v150, v44, v150
	v_mul_f32_e32 v44, v219, v192
	v_mul_f32_e32 v149, v44, v149
	v_mul_f32_e32 v44, v220, v192
	v_mul_f32_e32 v148, v44, v148
	v_mul_f32_e32 v44, v221, v192
	v_mul_f32_e32 v147, v44, v147
	v_mul_f32_e32 v44, v214, v192
	v_mul_f32_e32 v146, v44, v146
	v_mul_f32_e32 v44, v215, v192
	v_mul_f32_e32 v145, v44, v145
	v_mul_f32_e32 v44, v216, v192
	v_mul_f32_e32 v144, v44, v144
	v_mul_f32_e32 v44, v217, v192
	v_mul_f32_e32 v143, v44, v143
	v_mul_f32_e32 v44, v200, v192
	v_mul_f32_e32 v142, v44, v142
	v_mul_f32_e32 v44, v201, v192
	v_mul_f32_e32 v141, v44, v141
	v_mul_f32_e32 v44, v202, v192
	v_mul_f32_e32 v140, v44, v140
	v_mul_f32_e32 v44, v203, v192
	v_mul_f32_e32 v139, v44, v139
	v_mul_f32_e32 v44, v196, v192
	v_mul_f32_e32 v138, v44, v138
	v_mul_f32_e32 v44, v197, v192
	v_mul_f32_e32 v137, v44, v137
	v_mul_f32_e32 v44, v198, v192
	v_mul_f32_e32 v136, v44, v136
	v_mul_f32_e32 v44, v199, v192
	v_mul_f32_e32 v135, v44, v135
	s_waitcnt vmcnt(0)
	v_mul_f32_e32 v44, v192, v80
	v_mul_f32_e32 v80, v44, v134
	v_mul_f32_e32 v44, v192, v81
	v_mul_f32_e32 v81, v44, v133
	v_mul_f32_e32 v44, v192, v82
	v_mul_f32_e32 v82, v44, v132
	v_mul_f32_e32 v44, v192, v83
	v_mul_f32_e32 v83, v44, v131
	v_mul_f32_e32 v44, v192, v72
	v_mul_f32_e32 v72, v44, v129
	v_mul_f32_e32 v44, v192, v73
	v_mul_f32_e32 v73, v44, v128
	v_mul_f32_e32 v44, v192, v74
	v_mul_f32_e32 v74, v44, v127
	v_mul_f32_e32 v44, v192, v75
	v_mul_f32_e32 v75, v44, v126
	v_mul_f32_e32 v44, v192, v226
	v_mul_f32_e32 v126, v44, v191
	v_mul_f32_e32 v44, v192, v227
	v_mul_f32_e32 v127, v44, v190
	v_mul_f32_e32 v44, v192, v228
	v_mul_f32_e32 v128, v44, v189
	v_mul_f32_e32 v44, v192, v229
	v_mul_f32_e32 v129, v44, v188
	v_mul_f32_e32 v44, v192, v222
	v_mul_f32_e32 v131, v44, v187
	v_mul_f32_e32 v44, v192, v223
	v_mul_f32_e32 v132, v44, v186
	v_mul_f32_e32 v44, v192, v224
	v_mul_f32_e32 v133, v44, v185
	v_mul_f32_e32 v44, v192, v225
	v_pk_mul_f32 v[16:17], v[192:193], v[16:17] op_sel_hi:[0,1]
	v_mul_f32_e32 v230, v87, v192
	v_mul_f32_e32 v241, v70, v192
	v_mul_f32_e32 v134, v44, v184
	v_pk_mul_f32 v[50:51], v[50:51], v[124:125]
	v_mov_b32_e32 v44, v49
	v_pk_mul_f32 v[30:31], v[40:41], v[30:31]
	v_pk_mul_f32 v[40:41], v[16:17], v[94:95]
	v_mov_b32_e32 v16, v64
	v_mov_b32_e32 v17, v36
	v_mul_f32_e32 v175, v230, v175
	v_mul_f32_e32 v174, v233, v174
	v_mul_f32_e32 v230, v234, v171
	v_mul_f32_e32 v233, v238, v167
	v_mul_f32_e32 v234, v241, v166
	v_mov_b32_e32 v166, v36
	v_mov_b32_e32 v167, v64
	v_pk_mul_f32 v[44:45], v[192:193], v[44:45] op_sel_hi:[0,1]
	v_pk_mul_f32 v[16:17], v[50:51], v[16:17]
	v_pk_mul_f32 v[44:45], v[44:45], v[76:77]
	v_sub_f32_e32 v76, v17, v16
	v_pk_mul_f32 v[16:17], v[50:51], v[166:167]
	v_mov_b32_e32 v36, v65
	v_add_f32_e32 v50, v16, v17
	v_pk_mul_f32 v[16:17], v[44:45], v[36:37]
	v_mov_b32_e32 v64, v37
	v_pk_mul_f32 v[48:49], v[192:193], v[172:173] op_sel_hi:[0,1]
	v_sub_f32_e32 v36, v17, v16
	v_pk_mul_f32 v[16:17], v[44:45], v[64:65]
	v_pk_mul_f32 v[48:49], v[48:49], v[120:121]
	v_add_f32_e32 v51, v16, v17
	v_mov_b32_e32 v16, v66
	v_mov_b32_e32 v17, v38
	v_mul_f32_e32 v232, v237, v170
	v_mov_b32_e32 v170, v38
	v_mov_b32_e32 v171, v66
	v_pk_mul_f32 v[46:47], v[192:193], v[46:47] op_sel_hi:[0,1]
	v_pk_mul_f32 v[16:17], v[48:49], v[16:17]
	v_pk_mul_f32 v[46:47], v[46:47], v[122:123]
	v_sub_f32_e32 v64, v17, v16
	v_pk_mul_f32 v[16:17], v[48:49], v[170:171]
	v_mov_b32_e32 v38, v67
	v_add_f32_e32 v65, v16, v17
	v_pk_mul_f32 v[16:17], v[46:47], v[38:39]
	v_mov_b32_e32 v66, v39
	v_pk_mul_f32 v[52:53], v[192:193], v[194:195] op_sel_hi:[0,1]
	v_sub_f32_e32 v77, v17, v16
	v_pk_mul_f32 v[16:17], v[46:47], v[66:67]
	v_mul_f32_e32 v90, v90, v192
	v_mul_f32_e32 v91, v91, v192
	v_pk_mul_f32 v[52:53], v[52:53], v[118:119]
	v_add_f32_e32 v66, v16, v17
	v_mov_b32_e32 v16, v26
	v_mov_b32_e32 v17, v22
	v_mul_f32_e32 v213, v90, v182
	v_mul_f32_e32 v179, v91, v179
	v_mov_b32_e32 v90, v22
	v_mov_b32_e32 v91, v26
	v_pk_mul_f32 v[16:17], v[52:53], v[16:17]
	v_mov_b32_e32 v22, v27
	v_sub_f32_e32 v37, v17, v16
	v_pk_mul_f32 v[16:17], v[52:53], v[90:91]
	v_mov_b32_e32 v26, v23
	v_add_f32_e32 v52, v16, v17
	v_pk_mul_f32 v[16:17], v[54:55], v[22:23]
	v_mul_f32_e32 v88, v88, v192
	v_sub_f32_e32 v38, v17, v16
	v_pk_mul_f32 v[16:17], v[54:55], v[26:27]
	v_mul_f32_e32 v89, v89, v192
	v_add_f32_e32 v53, v16, v17
	v_mov_b32_e32 v16, v28
	v_mov_b32_e32 v17, v24
	v_mul_f32_e32 v183, v88, v183
	v_mul_f32_e32 v181, v89, v181
	v_mov_b32_e32 v88, v24
	v_mov_b32_e32 v89, v28
	v_pk_mul_f32 v[16:17], v[56:57], v[16:17]
	v_mov_b32_e32 v24, v29
	v_sub_f32_e32 v54, v17, v16
	v_pk_mul_f32 v[16:17], v[56:57], v[88:89]
	v_mov_b32_e32 v28, v25
	v_add_f32_e32 v55, v16, v17
	v_pk_mul_f32 v[16:17], v[42:43], v[24:25]
	v_mul_f32_e32 v86, v86, v192
	v_sub_f32_e32 v56, v17, v16
	v_pk_mul_f32 v[16:17], v[42:43], v[28:29]
	v_mul_f32_e32 v178, v86, v178
	v_add_f32_e32 v57, v16, v17
	v_mov_b32_e32 v16, v10
	v_mov_b32_e32 v17, v6
	v_mov_b32_e32 v86, v6
	v_mov_b32_e32 v87, v10
	v_pk_mul_f32 v[18:19], v[192:193], v[18:19] op_sel_hi:[0,1]
	v_pk_mul_f32 v[16:17], v[58:59], v[16:17]
	v_pk_mul_f32 v[18:19], v[18:19], v[112:113]
	v_sub_f32_e32 v39, v17, v16
	v_pk_mul_f32 v[16:17], v[58:59], v[86:87]
	v_mov_b32_e32 v6, v11
	v_mov_b32_e32 v10, v7
	v_mul_f32_e32 v84, v84, v192
	v_add_f32_e32 v58, v16, v17
	v_pk_mul_f32 v[16:17], v[18:19], v[6:7]
	v_pk_mul_f32 v[6:7], v[18:19], v[10:11]
	v_mul_f32_e32 v239, v68, v192
	v_mul_f32_e32 v240, v69, v192
	v_mul_f32_e32 v182, v84, v180
	v_add_f32_e32 v67, v6, v7
	v_mov_b32_e32 v6, v12
	v_mov_b32_e32 v7, v8
	v_mov_b32_e32 v180, v205
	v_mul_f32_e32 v242, v71, v192
	v_mov_b32_e32 v84, v8
	v_mov_b32_e32 v85, v12
	v_mul_f32_e32 v169, v236, v169
	v_mul_f32_e32 v168, v239, v168
	v_mul_f32_e32 v165, v240, v165
	v_pk_mul_f32 v[20:21], v[192:193], v[20:21] op_sel_hi:[0,1]
	v_pk_mul_f32 v[6:7], v[60:61], v[6:7]
	v_cvt_pk_fp8_f32 v180, v183, v181
	v_mov_b32_e32 v183, v205
	v_mov_b32_e32 v184, v205
	v_mul_f32_e32 v235, v242, v164
	v_pk_mul_f32 v[20:21], v[20:21], v[106:107]
	v_sub_f32_e32 v78, v7, v6
	v_pk_mul_f32 v[6:7], v[60:61], v[84:85]
	v_mov_b32_e32 v8, v13
	v_cvt_pk_fp8_f32 v183, v231, v169
	v_cvt_pk_fp8_f32 v184, v168, v165
	v_mov_b32_e32 v185, v205
	v_mov_b32_e32 v164, v162
	v_mov_b32_e32 v165, v162
	v_mov_b32_e32 v166, v162
	v_mov_b32_e32 v167, v162
	v_mov_b32_e32 v168, v162
	v_mov_b32_e32 v169, v162
	v_add_f32_e32 v60, v6, v7
	v_pk_mul_f32 v[6:7], v[20:21], v[8:9]
	v_mov_b32_e32 v12, v9
	v_cvt_pk_fp8_f32 v185, v163, v161
	v_mov_b32_e32 v163, v162
	v_mov_b64_e32 v[170:171], v[168:169]
	v_sub_f32_e32 v61, v7, v6
	v_pk_mul_f32 v[6:7], v[20:21], v[12:13]
	v_mov_b32_e32 v181, v205
	v_mov_b64_e32 v[168:169], v[166:167]
	v_mov_b64_e32 v[166:167], v[164:165]
	v_mov_b64_e32 v[164:165], v[162:163]
	s_cselect_b32 s7, s10, s12
	s_cselect_b32 s6, s9, s11
	s_add_i32 s13, s65, 0xb800
	v_add_f32_e32 v79, v6, v7
	v_mov_b32_e32 v6, v32
	v_mov_b32_e32 v7, v2
	v_cvt_pk_fp8_f32 v181, v182, v177
	v_mov_b32_e32 v182, v205
	v_mov_b32_e32 v186, v205
	v_mov_b32_e32 v187, v205
	s_mov_b32 s14, m0
	s_mov_b32 m0, s13
	s_nop 0
	global_load_lds_dwordx4 v211, s[6:7]
	s_mov_b32 m0, s14
	s_and_b64 s[6:7], exec, s[54:55]
	v_mov_b32_e32 v70, v2
	v_mov_b32_e32 v71, v32
	v_pk_mul_f32 v[14:15], v[192:193], v[14:15] op_sel_hi:[0,1]
	v_pk_mul_f32 v[6:7], v[62:63], v[6:7]
	v_cvt_pk_fp8_f32 v182, v176, v193
	v_cvt_pk_fp8_f32 v186, v158, v157
	s_cselect_b32 s7, s10, s12
	s_cselect_b32 s6, s9, s11
	s_add_i32 s9, s64, 0xb800
	s_mov_b32 s10, m0
	s_mov_b32 m0, s9
	s_nop 0
	global_load_lds_dwordx4 v210, s[6:7]
	s_mov_b32 m0, s10
	v_cvt_pk_fp8_f32 v187, v154, v153
	v_pk_mul_f32 v[14:15], v[14:15], v[100:101]
	v_sub_f32_e32 v84, v7, v6
	v_pk_mul_f32 v[6:7], v[62:63], v[70:71]
	v_mov_b32_e32 v2, v33
	s_add_i32 s9, s33, 0xb800
	s_mov_b32 s10, m0
	s_mov_b32 m0, s9
	s_nop 0
	global_load_lds_dwordx4 v212, s[6:7]
	s_mov_b32 m0, s10
	v_add_f32_e32 v62, v6, v7
	v_pk_mul_f32 v[6:7], v[14:15], v[2:3]
	v_mov_b32_e32 v32, v3
	v_cvt_pk_fp8_f32 v180, v213, v179 op_sel:[0,0,1]
	s_waitcnt vmcnt(0) lgkmcnt(0)
	s_barrier
	v_add_u32_e32 v213, 0, v204
	v_sub_f32_e32 v63, v7, v6
	v_pk_mul_f32 v[2:3], v[14:15], v[32:33]
	ds_read_b128 v[6:9], v213
	ds_read_b128 v[10:13], v213 offset:16
	v_add_f32_e32 v70, v2, v3
	v_mov_b32_e32 v2, v34
	v_mov_b32_e32 v3, v4
	v_cvt_pk_fp8_f32 v181, v178, v175 op_sel:[0,0,1]
	v_cvt_pk_fp8_f32 v182, v174, v230 op_sel:[0,0,1]
	v_cvt_pk_fp8_f32 v183, v232, v233 op_sel:[0,0,1]
	v_cvt_pk_fp8_f32 v184, v234, v235 op_sel:[0,0,1]
	v_cvt_pk_fp8_f32 v185, v160, v159 op_sel:[0,0,1]
	v_cvt_pk_fp8_f32 v186, v156, v155 op_sel:[0,0,1]
	v_cvt_pk_fp8_f32 v187, v152, v151 op_sel:[0,0,1]
	v_mov_b32_e32 v68, v4
	v_mov_b32_e32 v69, v34
	v_pk_mul_f32 v[2:3], v[30:31], v[2:3]
	v_mov_b32_e32 v4, v35
	v_sub_f32_e32 v71, v3, v2
	v_pk_mul_f32 v[2:3], v[30:31], v[68:69]
	v_mov_b32_e32 v34, v5
	v_add_f32_e32 v68, v2, v3
	v_pk_mul_f32 v[2:3], v[40:41], v[4:5]
	s_waitcnt lgkmcnt(0)
	v_mfma_f32_32x32x64_f8f6f4 v[18:33], v[6:13], v[180:187], 0
	v_sub_f32_e32 v69, v3, v2
	ds_read_b128 v[2:5], v213 offset:6656
	ds_read_b128 v[6:9], v213 offset:6672
	v_sub_f32_e32 v59, v17, v16
	v_mov_b32_e32 v188, v205
	v_mov_b32_e32 v189, v205
	v_mov_b32_e32 v190, v205
	v_mov_b32_e32 v191, v205
	v_mov_b32_e32 v192, v205
	v_mov_b32_e32 v193, v205
	v_mov_b32_e32 v194, v205
	v_mov_b32_e32 v195, v205
	v_cvt_pk_fp8_f32 v188, v150, v149
	v_cvt_pk_fp8_f32 v189, v146, v145
	v_cvt_pk_fp8_f32 v190, v142, v141
	v_cvt_pk_fp8_f32 v191, v138, v137
	s_waitcnt lgkmcnt(0)
	v_mfma_f32_32x32x64_f8f6f4 v[2:17], v[2:9], v[180:187], 0
	v_cvt_pk_fp8_f32 v192, v80, v81
	v_cvt_pk_fp8_f32 v193, v72, v73
	v_cvt_pk_fp8_f32 v194, v126, v127
	v_cvt_pk_fp8_f32 v195, v131, v132
	ds_read_b128 v[42:45], v213 offset:64
	ds_read_b128 v[46:49], v213 offset:80
	v_cvt_pk_fp8_f32 v188, v148, v147 op_sel:[0,0,1]
	v_cvt_pk_fp8_f32 v189, v144, v143 op_sel:[0,0,1]
	v_cvt_pk_fp8_f32 v190, v140, v139 op_sel:[0,0,1]
	v_cvt_pk_fp8_f32 v191, v136, v135 op_sel:[0,0,1]
	v_cvt_pk_fp8_f32 v192, v82, v83 op_sel:[0,0,1]
	v_cvt_pk_fp8_f32 v193, v74, v75 op_sel:[0,0,1]
	v_cvt_pk_fp8_f32 v194, v128, v129 op_sel:[0,0,1]
	v_cvt_pk_fp8_f32 v195, v133, v134 op_sel:[0,0,1]
	v_pk_mul_f32 v[34:35], v[40:41], v[34:35]
	v_mov_b32_e32 v196, v205
	v_mov_b32_e32 v197, v205
	v_mov_b32_e32 v198, v205
	v_add_f32_e32 v72, v34, v35
	s_waitcnt lgkmcnt(0)
	v_mfma_f32_32x32x64_f8f6f4 v[18:33], v[42:49], v[188:195], v[18:33]
	v_cvt_pk_fp8_f32 v196, v76, v36
	v_cvt_pk_fp8_f32 v197, v37, v38
	v_cvt_pk_fp8_f32 v198, v39, v59
	ds_read_b128 v[34:37], v213 offset:6720
	ds_read_b128 v[38:41], v213 offset:6736
	v_mov_b32_e32 v199, v205
	v_mov_b32_e32 v200, v205
	v_mov_b32_e32 v201, v205
	v_mov_b32_e32 v202, v205
	v_mov_b32_e32 v203, v205
	v_cvt_pk_fp8_f32 v199, v84, v63
	v_cvt_pk_fp8_f32 v200, v50, v51
	v_cvt_pk_fp8_f32 v201, v52, v53
	v_cvt_pk_fp8_f32 v202, v58, v67
	v_cvt_pk_fp8_f32 v203, v62, v70
	v_cvt_pk_fp8_f32 v196, v64, v77 op_sel:[0,0,1]
	s_waitcnt lgkmcnt(0)
	v_mfma_f32_32x32x64_f8f6f4 v[2:17], v[34:41], v[188:195], v[2:17]
	ds_read_b128 v[34:37], v213 offset:128
	ds_read_b128 v[38:41], v213 offset:144
	v_cvt_pk_fp8_f32 v197, v54, v56 op_sel:[0,0,1]
	v_cvt_pk_fp8_f32 v198, v78, v61 op_sel:[0,0,1]
	v_cvt_pk_fp8_f32 v199, v71, v69 op_sel:[0,0,1]
	v_cvt_pk_fp8_f32 v200, v65, v66 op_sel:[0,0,1]
	v_cvt_pk_fp8_f32 v201, v55, v57 op_sel:[0,0,1]
	v_cvt_pk_fp8_f32 v202, v60, v79 op_sel:[0,0,1]
	v_cvt_pk_fp8_f32 v203, v68, v72 op_sel:[0,0,1]
	s_mov_b32 s9, s8
	s_mov_b32 s10, s8
	s_mov_b32 s11, s8
	s_mov_b32 s12, s8
	s_mov_b32 s13, s8
	s_mov_b32 s14, s8
	v_mov_b64_e32 v[80:81], s[22:23]
	s_waitcnt lgkmcnt(0)
	v_mfma_f32_32x32x64_f8f6f4 v[18:33], v[34:41], v[196:203], v[18:33]
	ds_read_b128 v[34:37], v213 offset:6784
	ds_read_b128 v[38:41], v213 offset:6800
	v_mov_b64_e32 v[78:79], s[20:21]
	v_mov_b64_e32 v[76:77], s[18:19]
	v_mov_b64_e32 v[74:75], s[16:17]
	v_mov_b64_e32 v[72:73], s[14:15]
	v_mov_b64_e32 v[70:71], s[12:13]
	v_mov_b64_e32 v[68:69], s[10:11]
	v_mov_b64_e32 v[66:67], s[8:9]
	s_add_u32 s10, s58, 0x8000
	s_addc_u32 s11, s59, 0
	v_mad_u32_u24 v163, v206, s89, v130
	s_add_u32 s12, s56, 0x200000
	v_mov_b64_e32 v[50:51], v[66:67]
	v_add_u32_e32 v214, 0, v163
	v_lshl_add_u32 v209, v206, 2, s51
	s_waitcnt lgkmcnt(0)
	v_mfma_f32_32x32x64_f8f6f4 v[2:17], v[34:41], v[196:203], v[2:17]
	s_nop 1
	v_max_f32_e32 v34, v19, v19
	v_max_f32_e32 v35, v18, v18
	v_max_f32_e32 v34, v35, v34
	v_lshlrev_b32_e32 v208, 4, v207
	s_addc_u32 s13, s57, 0
	s_mov_b32 s9, 0
	s_mov_b32 s14, -1
	v_mov_b32_e32 v172, 0
	v_mov_b32_e32 v173, 0
	v_mov_b32_e32 v174, 0
	v_mov_b32_e32 v175, 0
	v_mov_b32_e32 v176, 0
	v_mov_b32_e32 v177, 0
	v_mov_b32_e32 v178, 0
	v_mov_b32_e32 v179, 0
	s_nop 2
	v_max3_f32 v35, v20, v21, v3
	v_max3_f32 v34, v34, v2, v4
	v_max3_f32 v34, v34, v5, v22
	v_max3_f32 v35, v35, v24, v25
	v_max3_f32 v34, v34, v23, v6
	v_max3_f32 v35, v35, v8, v9
	v_max3_f32 v34, v34, v7, v26
	v_max3_f32 v35, v35, v28, v29
	v_max3_f32 v34, v34, v27, v10
	v_max3_f32 v35, v35, v12, v13
	v_max3_f32 v34, v34, v11, v30
	v_max3_f32 v35, v35, v32, v33
	v_max3_f32 v34, v34, v31, v14
	v_max3_f32 v35, v35, v16, v17
	v_max3_f32 v34, v34, v15, v35
	v_mov_b32_e32 v35, v34
	s_nop 1
	v_permlane32_swap_b32_e32 v34, v35
	v_max_f32 v34, v34, v35
	v_mov_b64_e32 v[52:53], v[68:69]
	v_add_f32_e32 v34, 0xc0e00000, v34
	v_sub_f32_e32 v82, 0, v34
	v_sub_f32_e32 v113, v33, v34
	v_sub_f32_e32 v112, v32, v34
	v_sub_f32_e32 v111, v31, v34
	v_sub_f32_e32 v110, v30, v34
	v_sub_f32_e32 v109, v29, v34
	v_sub_f32_e32 v108, v28, v34
	v_sub_f32_e32 v107, v27, v34
	v_sub_f32_e32 v106, v26, v34
	v_sub_f32_e32 v105, v25, v34
	v_sub_f32_e32 v104, v24, v34
	v_sub_f32_e32 v103, v23, v34
	v_sub_f32_e32 v102, v22, v34
	v_sub_f32_e32 v101, v21, v34
	v_sub_f32_e32 v100, v20, v34
	v_sub_f32_e32 v99, v19, v34
	v_sub_f32_e32 v98, v18, v34
	v_sub_f32_e32 v129, v17, v34
	v_sub_f32_e32 v128, v16, v34
	v_sub_f32_e32 v127, v15, v34
	v_sub_f32_e32 v126, v14, v34
	v_sub_f32_e32 v125, v13, v34
	v_sub_f32_e32 v124, v12, v34
	v_sub_f32_e32 v123, v11, v34
	v_sub_f32_e32 v122, v10, v34
	v_sub_f32_e32 v121, v9, v34
	v_sub_f32_e32 v120, v8, v34
	v_sub_f32_e32 v119, v7, v34
	v_sub_f32_e32 v118, v6, v34
	v_sub_f32_e32 v117, v5, v34
	v_sub_f32_e32 v116, v4, v34
	v_sub_f32_e32 v115, v3, v34
	v_sub_f32_e32 v114, v2, v34
	v_mov_b64_e32 v[2:3], v[66:67]
	v_mov_b64_e32 v[18:19], v[66:67]
	v_mov_b64_e32 v[34:35], v[66:67]
	v_mov_b32_e32 v83, v82
	v_mov_b32_e32 v84, v82
	v_mov_b32_e32 v85, v82
	v_mov_b32_e32 v86, v82
	v_mov_b32_e32 v87, v82
	v_mov_b32_e32 v88, v82
	v_mov_b32_e32 v89, v82
	v_mov_b32_e32 v90, v82
	v_mov_b32_e32 v91, v82
	v_mov_b32_e32 v92, v82
	v_mov_b32_e32 v93, v82
	v_mov_b32_e32 v94, v82
	v_mov_b32_e32 v95, v82
	v_mov_b32_e32 v96, v82
	v_mov_b32_e32 v97, v82
	v_mov_b64_e32 v[4:5], v[68:69]
	v_mov_b64_e32 v[6:7], v[70:71]
	v_mov_b64_e32 v[8:9], v[72:73]
	v_mov_b64_e32 v[10:11], v[74:75]
	v_mov_b64_e32 v[12:13], v[76:77]
	v_mov_b64_e32 v[14:15], v[78:79]
	v_mov_b64_e32 v[16:17], v[80:81]
	v_mov_b64_e32 v[20:21], v[68:69]
	v_mov_b64_e32 v[22:23], v[70:71]
	v_mov_b64_e32 v[24:25], v[72:73]
	v_mov_b64_e32 v[26:27], v[74:75]
	v_mov_b64_e32 v[28:29], v[76:77]
	v_mov_b64_e32 v[30:31], v[78:79]
	v_mov_b64_e32 v[32:33], v[80:81]
	v_mov_b64_e32 v[36:37], v[68:69]
	v_mov_b64_e32 v[38:39], v[70:71]
	v_mov_b64_e32 v[40:41], v[72:73]
	v_mov_b64_e32 v[42:43], v[74:75]
	v_mov_b64_e32 v[44:45], v[76:77]
	v_mov_b64_e32 v[46:47], v[78:79]
	v_mov_b64_e32 v[48:49], v[80:81]
	v_mov_b64_e32 v[54:55], v[70:71]
	v_mov_b64_e32 v[56:57], v[72:73]
	v_mov_b64_e32 v[58:59], v[74:75]
	v_mov_b64_e32 v[60:61], v[76:77]
	v_mov_b64_e32 v[62:63], v[78:79]
	v_mov_b64_e32 v[64:65], v[80:81]
	v_readfirstlane_b32 s100, v0
	s_nop 3
	s_lshr_b32 s100, s100, 8
	s_cmp_eq_u32 s100, 0
	s_cbranch_scc1 .Lmla_prio_lead
	s_setprio 1
.Lmla_prio_lead:
.LBB0_558:
	s_mul_i32 s6, s9, 0x5c00
	s_add_i32 s7, s6, 0x5c00
	s_cmp_lt_i32 s9, 4
	s_cselect_b32 s7, s7, 0
	s_add_i32 s15, s7, 0
	v_add_u32_e32 v215, s15, v204
	ds_read_b128 v[216:219], v215
	ds_read_b128 v[220:223], v215 offset:16
	ds_read_b128 v[224:227], v215 offset:6656
	ds_read_b128 v[228:231], v215 offset:6672
	ds_read_b128 v[232:235], v215 offset:64
	ds_read_b128 v[236:239], v215 offset:80
	ds_read_b128 v[240:243], v215 offset:6720
	ds_read_b128 v[244:247], v215 offset:6736
	v_add_u32_e32 v248, s6, v214
	s_cmp_gt_i32 s9, 1
	s_cselect_b32 s7, -2, 3
	s_add_i32 s7, s7, s9
	s_add_u32 s18, s12, 0xfff80000
	s_addc_u32 s19, s13, -1
	s_add_u32 s20, s10, 0xffffe000
	s_addc_u32 s21, s11, -1
	s_mulk_i32 s7, 0x5c00
	v_exp_f32_e32 v98, v98
	v_exp_f32_e32 v99, v99
	v_exp_f32_e32 v100, v100
	v_exp_f32_e32 v101, v101
	v_exp_f32_e32 v102, v102
	v_exp_f32_e32 v103, v103
	v_exp_f32_e32 v104, v104
	v_exp_f32_e32 v105, v105
	s_waitcnt lgkmcnt(6)
	v_mfma_f32_32x32x64_f8f6f4 v[146:161], v[216:223], v[180:187], v[82:97]
	ds_read_b128 v[216:219], v215 offset:128
	ds_read_b128 v[220:223], v215 offset:144
	v_exp_f32_e32 v106, v106
	v_exp_f32_e32 v107, v107
	v_exp_f32_e32 v108, v108
	v_exp_f32_e32 v109, v109
	v_exp_f32_e32 v110, v110
	v_cvt_pk_fp8_f32 v172, v98, v99
	v_cvt_pk_fp8_f32 v173, v102, v103
	s_waitcnt lgkmcnt(6)
	v_mfma_f32_32x32x64_f8f6f4 v[130:145], v[224:231], v[180:187], v[82:97]
	ds_read_b128 v[224:227], v215 offset:6784
	ds_read_b128 v[228:231], v215 offset:6800
	v_exp_f32_e32 v111, v111
	v_exp_f32_e32 v112, v112
	v_exp_f32_e32 v113, v113
	v_exp_f32_e32 v114, v114
	v_exp_f32_e32 v115, v115
	v_cvt_pk_fp8_f32 v172, v100, v101 op_sel:[0,0,1]
	v_cvt_pk_fp8_f32 v173, v104, v105 op_sel:[0,0,1]
	s_waitcnt lgkmcnt(6)
	v_mfma_f32_32x32x64_f8f6f4 v[146:161], v[232:239], v[188:195], v[146:161]
	ds_read_b128 v[232:235], v248 offset:13312
	ds_read_b128 v[236:239], v248 offset:13328
	v_exp_f32_e32 v116, v116
	v_exp_f32_e32 v117, v117
	v_exp_f32_e32 v118, v118
	v_exp_f32_e32 v119, v119
	v_exp_f32_e32 v120, v120
	v_cvt_pk_fp8_f32 v174, v106, v107
	v_cvt_pk_fp8_f32 v174, v108, v109 op_sel:[0,0,1]
	v_cvt_pk_fp8_f32 v175, v110, v111
	s_waitcnt lgkmcnt(6)
	v_mfma_f32_32x32x64_f8f6f4 v[130:145], v[240:247], v[188:195], v[130:145]
	ds_read_b128 v[240:243], v248 offset:15872
	ds_read_b128 v[244:247], v248 offset:15888
	v_exp_f32_e32 v121, v121
	v_exp_f32_e32 v122, v122
	v_exp_f32_e32 v123, v123
	v_exp_f32_e32 v124, v124
	v_exp_f32_e32 v125, v125
	v_cvt_pk_fp8_f32 v175, v112, v113 op_sel:[0,0,1]
	v_cvt_pk_fp8_f32 v176, v114, v115
	v_cvt_pk_fp8_f32 v176, v116, v117 op_sel:[0,0,1]
	s_waitcnt lgkmcnt(6)
	v_mfma_f32_32x32x64_f8f6f4 v[146:161], v[216:223], v[196:203], v[146:161]
	ds_read_b128 v[216:219], v248 offset:18432
	ds_read_b128 v[220:223], v248 offset:18448
	v_exp_f32_e32 v126, v126
	v_exp_f32_e32 v127, v127
	v_exp_f32_e32 v128, v128
	v_exp_f32_e32 v129, v129
	v_cvt_pk_fp8_f32 v177, v118, v119
	v_cvt_pk_fp8_f32 v177, v120, v121 op_sel:[0,0,1]
	v_cvt_pk_fp8_f32 v178, v122, v123
	v_cvt_pk_fp8_f32 v178, v124, v125 op_sel:[0,0,1]
	s_waitcnt lgkmcnt(6)
	v_mfma_f32_32x32x64_f8f6f4 v[130:145], v[224:231], v[196:203], v[130:145]
	ds_read_b128 v[224:227], v248 offset:20992
	ds_read_b128 v[228:231], v248 offset:21008
	v_cvt_pk_fp8_f32 v179, v126, v127
	v_cvt_pk_fp8_f32 v179, v128, v129 op_sel:[0,0,1]
	s_and_b64 s[16:17], s[52:53], exec
	s_cselect_b32 s17, s19, s21
	s_cselect_b32 s16, s18, s20
	s_add_i32 s22, s7, s65
	s_mov_b32 s23, m0
	s_mov_b32 m0, s22
	s_nop 0
	global_load_lds_dwordx4 v211, s[16:17]
	s_waitcnt lgkmcnt(6)
	v_mfma_f32_32x32x64_f8f6f4 v[50:65], v[172:179], v[232:239], v[50:65]
	s_cmp_gt_i32 s9, 2
	s_cselect_b32 s98, -3, 2
	s_add_i32 s98, s98, s9
	s_mul_i32 s98, s98, 0x5c00
	v_add_u32_e32 v249, s98, v213
	ds_read_b128 v[232:235], v249
	ds_read_b128 v[236:239], v249 offset:16
	s_and_b64 s[16:17], exec, s[54:55]
	s_cselect_b32 s17, s19, s21
	s_cselect_b32 s16, s18, s20
	s_add_i32 s18, s7, s64
	s_mov_b32 m0, s18
	s_nop 0
	global_load_lds_dwordx4 v210, s[16:17]
	s_waitcnt lgkmcnt(6)
	v_mfma_f32_32x32x64_f8f6f4 v[34:49], v[172:179], v[240:247], v[34:49]
	ds_read_b128 v[240:243], v249 offset:6656
	ds_read_b128 v[244:247], v249 offset:6672
	s_add_i32 s7, s7, s33
	s_mov_b32 m0, s7
	s_nop 0
	global_load_lds_dwordx4 v212, s[16:17]
	s_waitcnt lgkmcnt(6)
	v_mfma_f32_32x32x64_f8f6f4 v[18:33], v[172:179], v[216:223], v[18:33]
	s_add_i32 s7, s6, 0xffffa400
	s_cmp_gt_i32 s9, 0
	s_cselect_b32 s7, s7, 0x17000
	s_and_b64 s[16:17], s[52:53], exec
	s_cselect_b32 s17, s13, s11
	s_cselect_b32 s16, s12, s10
	s_add_i32 s18, s7, s65
	s_mov_b32 m0, s18
	s_nop 0
	global_load_lds_dwordx4 v211, s[16:17]
	v_max3_f32 v98, v146, v147, v148
	v_max3_f32 v99, v149, v150, v151
	v_max3_f32 v98, v98, v152, v153
	v_max3_f32 v99, v99, v154, v155
	v_max3_f32 v98, v98, v156, v157
	v_max3_f32 v99, v99, v158, v159
	s_waitcnt lgkmcnt(4)
	v_mfma_f32_32x32x64_f8f6f4 v[2:17], v[172:179], v[224:231], v[2:17]
	s_and_b64 s[16:17], exec, s[54:55]
	s_cselect_b32 s17, s13, s11
	s_cselect_b32 s16, s12, s10
	s_add_i32 s18, s7, s64
	s_mov_b32 m0, s18
	s_nop 0
	global_load_lds_dwordx4 v210, s[16:17]
	v_max3_f32 v98, v98, v160, v161
	v_max3_f32 v99, v99, v130, v131
	v_max3_f32 v98, v98, v132, v133
	v_max3_f32 v99, v99, v134, v135
	v_max3_f32 v98, v98, v136, v137
	v_max3_f32 v99, v99, v138, v139
	v_mfma_f32_32x32x64_f8f6f4 v[66:81], v[172:179], v[164:171], v[66:81]
	s_add_i32 s7, s7, s33
	s_mov_b32 m0, s7
	s_nop 0
	global_load_lds_dwordx4 v212, s[16:17]
	s_mov_b32 m0, s23
	v_max3_f32 v98, v98, v140, v141
	v_max3_f32 v99, v99, v142, v143
	v_max3_f32 v98, v98, v144, v145
	v_max_f32_e32 v98, v98, v99
	v_mov_b32_e32 v99, v98
	s_nop 1
	v_permlane32_swap_b32_e32 v98, v99
	v_max_f32_e32 v98, v98, v99
	s_nop 0
	v_cmp_ge_f32_e64 s[6:7], s90, v98
	s_cmp_eq_u64 s[6:7], exec
	s_cbranch_scc0 .LBB0_561

.LBB0_560:
	s_add_u32 s10, s10, 0x4000
	s_addc_u32 s11, s11, 0
	s_add_u32 s12, s12, 0x100000
	s_waitcnt vmcnt(0) lgkmcnt(0)
	s_barrier
	s_addc_u32 s13, s13, 0
	s_add_i32 s14, s14, 2
	s_cmpk_lt_u32 s14, 0xff
	s_cbranch_scc1 .LBB0_558
	s_setprio 0
	s_branch .LBB0_567
